# GEMM_OUT epilogues (layers > 0): each residual batch's vmcnt(0) replaced by counted waits at the first consumer of every piece
# speedup vs baseline: 1.0031x; 1.0031x over previous
.Lpeel_exit_1:
	s_lshl_b32 s0, s78, 8
	s_add_i32 s41, s0, s13
	s_cmpk_lt_i32 s41, 0x2000
	s_cselect_b64 s[0:1], -1, 0
	s_add_i32 s36, s41, 0xffffe000
	s_lshr_b32 s42, s36, 11
	s_and_b64 s[36:37], s[0:1], exec
	s_cselect_b32 s36, 32, s42
	s_ashr_i32 s37, s41, 31
	s_and_b64 s[0:1], s[0:1], exec
	s_cselect_b32 s1, s37, 0
	s_cselect_b32 s0, s41, s41
	s_lshl_b64 s[0:1], s[0:1], 11
	s_mul_hi_u32 s37, s36, 0x6000
	s_mulk_i32 s36, 0x6000
	s_add_u32 s36, s63, s36
	s_addc_u32 s37, s64, s37
	s_nop 7
	s_nop 7
	s_nop 3
	s_mov_b32 s40, 0
	v_lshl_or_b32 v18, s77, 8, v180
	s_add_u32 s0, s59, s0
	v_add_u32_e32 v20, s40, v178
	v_ashrrev_i32_e32 v19, 31, v18
	s_addc_u32 s1, s62, s1
	v_ashrrev_i32_e32 v21, 31, v20
	v_lshl_add_u64 v[6:7], v[18:19], 2, s[36:37]
	v_lshl_add_u64 v[18:19], v[18:19], 1, s[0:1]
	v_lshlrev_b64 v[20:21], 11, v[20:21]
	v_lshl_add_u64 v[18:19], v[18:19], 0, v[20:21]
	s_mov_b64 s[0:1], 0x8000
	v_lshl_add_u64 v[202:203], v[18:19], 0, s[0:1]
	s_mov_b32 s0, 0x8000
	v_add_co_u32_e32 v204, vcc, s0, v18
	s_mov_b64 s[0:1], 0x10000
	s_nop 0
	v_addc_co_u32_e32 v205, vcc, 0, v19, vcc
	v_lshl_add_u64 v[206:207], v[18:19], 0, s[0:1]
	s_mov_b32 s0, 0x10000
	v_add_co_u32_e32 v208, vcc, s0, v18
	s_mov_b64 s[0:1], 0x18000
	s_nop 0
	v_addc_co_u32_e32 v209, vcc, 0, v19, vcc
	v_lshl_add_u64 v[20:21], v[18:19], 0, s[0:1]
	s_mov_b32 s0, 0x18000
	global_load_dwordx4 v[10:13], v[6:7], off offset:16
	global_load_dwordx4 v[14:17], v[6:7], off
	global_load_dwordx4 v[2:5], v[6:7], off offset:528
	s_nop 0
	global_load_dwordx4 v[6:9], v[6:7], off offset:512
	v_add_co_u32_e32 v210, vcc, s0, v18
	global_load_dwordx4 v[22:25], v[18:19], off
	global_load_dwordx4 v[26:29], v[18:19], off offset:256
	v_addc_co_u32_e32 v211, vcc, 0, v19, vcc
	global_load_dwordx4 v[30:33], v[204:205], off
	global_load_dwordx4 v[182:185], v[202:203], off offset:256
	global_load_dwordx4 v[186:189], v[208:209], off
	global_load_dwordx4 v[190:193], v[206:207], off offset:256
	global_load_dwordx4 v[194:197], v[210:211], off
	global_load_dwordx4 v[198:201], v[20:21], off offset:256
	s_waitcnt vmcnt(7)
	v_lshlrev_b32_e32 v214, 16, v22
	v_and_b32_e32 v215, 0xffff0000, v22
	v_lshlrev_b32_e32 v22, 16, v23
	v_and_b32_e32 v23, 0xffff0000, v23
	v_lshlrev_b32_e32 v218, 16, v24
	v_and_b32_e32 v219, 0xffff0000, v24
	v_lshlrev_b32_e32 v24, 16, v25
	v_and_b32_e32 v25, 0xffff0000, v25
	v_pk_fma_f32 v[162:163], v[162:163], v[16:17], v[22:23]
	v_pk_fma_f32 v[22:23], v[160:161], v[14:15], v[214:215]
	v_pk_fma_f32 v[158:159], v[158:159], v[12:13], v[24:25]
	v_pk_fma_f32 v[24:25], v[156:157], v[10:11], v[218:219]
	v_cvt_pk_bf16_f32 v22, v22, v23
	v_cvt_pk_bf16_f32 v23, v162, v163
	v_cvt_pk_bf16_f32 v24, v24, v25
	v_cvt_pk_bf16_f32 v25, v158, v159
	global_store_dwordx4 v[18:19], v[22:25], off
	s_nop 1
	s_waitcnt vmcnt(7)
	v_lshlrev_b32_e32 v22, 16, v26
	v_and_b32_e32 v23, 0xffff0000, v26
	v_lshlrev_b32_e32 v24, 16, v27
	v_and_b32_e32 v25, 0xffff0000, v27
	v_lshlrev_b32_e32 v26, 16, v28
	v_and_b32_e32 v27, 0xffff0000, v28
	v_lshlrev_b32_e32 v28, 16, v29
	v_and_b32_e32 v29, 0xffff0000, v29
	v_pk_fma_f32 v[24:25], v[154:155], v[8:9], v[24:25]
	v_pk_fma_f32 v[22:23], v[152:153], v[6:7], v[22:23]
	v_pk_fma_f32 v[28:29], v[146:147], v[4:5], v[28:29]
	v_pk_fma_f32 v[26:27], v[144:145], v[2:3], v[26:27]
	v_cvt_pk_bf16_f32 v22, v22, v23
	v_cvt_pk_bf16_f32 v23, v24, v25
	v_cvt_pk_bf16_f32 v24, v26, v27
	v_cvt_pk_bf16_f32 v25, v28, v29
	global_store_dwordx4 v[18:19], v[22:25], off offset:256
	s_waitcnt vmcnt(7)
	v_lshlrev_b32_e32 v26, 16, v32
	v_and_b32_e32 v27, 0xffff0000, v32
	v_lshlrev_b32_e32 v22, 16, v30
	v_and_b32_e32 v23, 0xffff0000, v30
	v_lshlrev_b32_e32 v24, 16, v31
	v_and_b32_e32 v25, 0xffff0000, v31
	v_lshlrev_b32_e32 v28, 16, v33
	v_and_b32_e32 v29, 0xffff0000, v33
	v_pk_fma_f32 v[24:25], v[150:151], v[16:17], v[24:25]
	v_pk_fma_f32 v[22:23], v[148:149], v[14:15], v[22:23]
	v_pk_fma_f32 v[28:29], v[142:143], v[12:13], v[28:29]
	v_pk_fma_f32 v[26:27], v[140:141], v[10:11], v[26:27]
	v_cvt_pk_bf16_f32 v22, v22, v23
	v_cvt_pk_bf16_f32 v23, v24, v25
	v_cvt_pk_bf16_f32 v24, v26, v27
	v_cvt_pk_bf16_f32 v25, v28, v29
	global_store_dwordx4 v[204:205], v[22:25], off
	s_waitcnt vmcnt(7)
	v_lshlrev_b32_e32 v26, 16, v184
	v_and_b32_e32 v27, 0xffff0000, v184
	v_lshlrev_b32_e32 v22, 16, v182
	v_and_b32_e32 v23, 0xffff0000, v182
	v_lshlrev_b32_e32 v24, 16, v183
	v_and_b32_e32 v25, 0xffff0000, v183
	v_lshlrev_b32_e32 v28, 16, v185
	v_and_b32_e32 v29, 0xffff0000, v185
	v_pk_fma_f32 v[24:25], v[138:139], v[8:9], v[24:25]
	v_pk_fma_f32 v[22:23], v[136:137], v[6:7], v[22:23]
	v_pk_fma_f32 v[28:29], v[130:131], v[4:5], v[28:29]
	v_pk_fma_f32 v[26:27], v[128:129], v[2:3], v[26:27]
	v_cvt_pk_bf16_f32 v22, v22, v23
	v_cvt_pk_bf16_f32 v23, v24, v25
	v_cvt_pk_bf16_f32 v24, v26, v27
	v_cvt_pk_bf16_f32 v25, v28, v29
	global_store_dwordx4 v[202:203], v[22:25], off offset:256
	s_waitcnt vmcnt(7)
	v_lshlrev_b32_e32 v26, 16, v188
	v_and_b32_e32 v27, 0xffff0000, v188
	v_lshlrev_b32_e32 v22, 16, v186
	v_and_b32_e32 v23, 0xffff0000, v186
	v_lshlrev_b32_e32 v24, 16, v187
	v_and_b32_e32 v25, 0xffff0000, v187
	v_lshlrev_b32_e32 v28, 16, v189
	v_and_b32_e32 v29, 0xffff0000, v189
	v_pk_fma_f32 v[24:25], v[134:135], v[16:17], v[24:25]
	v_pk_fma_f32 v[22:23], v[132:133], v[14:15], v[22:23]
	v_pk_fma_f32 v[28:29], v[126:127], v[12:13], v[28:29]
	v_pk_fma_f32 v[26:27], v[124:125], v[10:11], v[26:27]
	v_cvt_pk_bf16_f32 v22, v22, v23
	v_cvt_pk_bf16_f32 v23, v24, v25
	v_cvt_pk_bf16_f32 v24, v26, v27
	v_cvt_pk_bf16_f32 v25, v28, v29
	global_store_dwordx4 v[208:209], v[22:25], off
	s_waitcnt vmcnt(7)
	v_lshlrev_b32_e32 v26, 16, v192
	v_and_b32_e32 v27, 0xffff0000, v192
	v_lshlrev_b32_e32 v22, 16, v190
	v_and_b32_e32 v23, 0xffff0000, v190
	v_lshlrev_b32_e32 v24, 16, v191
	v_and_b32_e32 v25, 0xffff0000, v191
	v_lshlrev_b32_e32 v28, 16, v193
	v_and_b32_e32 v29, 0xffff0000, v193
	v_pk_fma_f32 v[24:25], v[122:123], v[8:9], v[24:25]
	v_pk_fma_f32 v[22:23], v[120:121], v[6:7], v[22:23]
	v_pk_fma_f32 v[28:29], v[114:115], v[4:5], v[28:29]
	v_pk_fma_f32 v[26:27], v[112:113], v[2:3], v[26:27]
	v_cvt_pk_bf16_f32 v22, v22, v23
	v_cvt_pk_bf16_f32 v23, v24, v25
	v_cvt_pk_bf16_f32 v24, v26, v27
	v_cvt_pk_bf16_f32 v25, v28, v29
	global_store_dwordx4 v[206:207], v[22:25], off offset:256
	s_waitcnt vmcnt(7)
	v_lshlrev_b32_e32 v26, 16, v196
	v_and_b32_e32 v27, 0xffff0000, v196
	v_lshlrev_b32_e32 v22, 16, v194
	v_and_b32_e32 v23, 0xffff0000, v194
	v_lshlrev_b32_e32 v24, 16, v195
	v_and_b32_e32 v25, 0xffff0000, v195
	v_lshlrev_b32_e32 v28, 16, v197
	v_and_b32_e32 v29, 0xffff0000, v197
	v_pk_fma_f32 v[24:25], v[118:119], v[16:17], v[24:25]
	v_pk_fma_f32 v[22:23], v[116:117], v[14:15], v[22:23]
	v_pk_fma_f32 v[28:29], v[110:111], v[12:13], v[28:29]
	v_pk_fma_f32 v[26:27], v[108:109], v[10:11], v[26:27]
	v_cvt_pk_bf16_f32 v22, v22, v23
	v_cvt_pk_bf16_f32 v23, v24, v25
	v_cvt_pk_bf16_f32 v24, v26, v27
	v_cvt_pk_bf16_f32 v25, v28, v29
	global_store_dwordx4 v[210:211], v[22:25], off
	s_waitcnt vmcnt(7)
	v_lshlrev_b32_e32 v26, 16, v200
	v_and_b32_e32 v27, 0xffff0000, v200
	v_lshlrev_b32_e32 v22, 16, v198
	v_and_b32_e32 v23, 0xffff0000, v198
	v_lshlrev_b32_e32 v24, 16, v199
	v_and_b32_e32 v25, 0xffff0000, v199
	v_lshlrev_b32_e32 v28, 16, v201
	v_and_b32_e32 v29, 0xffff0000, v201
	v_pk_fma_f32 v[24:25], v[106:107], v[8:9], v[24:25]
	v_pk_fma_f32 v[22:23], v[104:105], v[6:7], v[22:23]
	v_pk_fma_f32 v[28:29], v[102:103], v[4:5], v[28:29]
	v_pk_fma_f32 v[26:27], v[100:101], v[2:3], v[26:27]
	v_cvt_pk_bf16_f32 v22, v22, v23
	v_cvt_pk_bf16_f32 v23, v24, v25
	v_cvt_pk_bf16_f32 v24, v26, v27
	v_cvt_pk_bf16_f32 v25, v28, v29
	global_store_dwordx4 v[20:21], v[22:25], off offset:256
	s_mov_b64 s[0:1], 0x40000
	v_lshl_add_u64 v[120:121], v[18:19], 0, s[0:1]
	s_mov_b32 s0, 0x40000
	v_add_co_u32_e32 v122, vcc, s0, v18
	s_mov_b64 s[0:1], 0x48000
	s_nop 0
	v_addc_co_u32_e32 v123, vcc, 0, v19, vcc
	v_lshl_add_u64 v[124:125], v[18:19], 0, s[0:1]
	s_mov_b32 s0, 0x48000
	v_add_co_u32_e32 v126, vcc, s0, v18
	s_mov_b64 s[0:1], 0x50000
	s_nop 0
	v_addc_co_u32_e32 v127, vcc, 0, v19, vcc
	v_lshl_add_u64 v[128:129], v[18:19], 0, s[0:1]
	s_mov_b32 s0, 0x50000
	v_add_co_u32_e32 v130, vcc, s0, v18
	s_mov_b64 s[0:1], 0x58000
	s_nop 0
	v_addc_co_u32_e32 v131, vcc, 0, v19, vcc
	v_lshl_add_u64 v[20:21], v[18:19], 0, s[0:1]
	s_mov_b32 s0, 0x58000
	v_add_co_u32_e32 v18, vcc, s0, v18
	global_load_dwordx4 v[22:25], v[122:123], off
	global_load_dwordx4 v[26:29], v[120:121], off offset:256
	v_addc_co_u32_e32 v19, vcc, 0, v19, vcc
	global_load_dwordx4 v[30:33], v[126:127], off
	global_load_dwordx4 v[100:103], v[124:125], off offset:256
	global_load_dwordx4 v[104:107], v[130:131], off
	global_load_dwordx4 v[108:111], v[128:129], off offset:256
	global_load_dwordx4 v[112:115], v[18:19], off
	global_load_dwordx4 v[116:119], v[20:21], off offset:256
	s_waitcnt vmcnt(7)
	v_lshlrev_b32_e32 v132, 16, v22
	v_and_b32_e32 v133, 0xffff0000, v22
	v_lshlrev_b32_e32 v22, 16, v23
	v_and_b32_e32 v23, 0xffff0000, v23
	v_lshlrev_b32_e32 v134, 16, v24
	v_and_b32_e32 v135, 0xffff0000, v24
	v_lshlrev_b32_e32 v24, 16, v25
	v_and_b32_e32 v25, 0xffff0000, v25
	v_pk_fma_f32 v[98:99], v[98:99], v[16:17], v[22:23]
	v_pk_fma_f32 v[22:23], v[96:97], v[14:15], v[132:133]
	v_pk_fma_f32 v[94:95], v[94:95], v[12:13], v[24:25]
	v_pk_fma_f32 v[24:25], v[92:93], v[10:11], v[134:135]
	v_cvt_pk_bf16_f32 v22, v22, v23
	v_cvt_pk_bf16_f32 v23, v98, v99
	v_cvt_pk_bf16_f32 v24, v24, v25
	v_cvt_pk_bf16_f32 v25, v94, v95
	global_store_dwordx4 v[122:123], v[22:25], off
	s_nop 1
	s_waitcnt vmcnt(7)
	v_lshlrev_b32_e32 v22, 16, v26
	v_and_b32_e32 v23, 0xffff0000, v26
	v_lshlrev_b32_e32 v24, 16, v27
	v_and_b32_e32 v25, 0xffff0000, v27
	v_lshlrev_b32_e32 v26, 16, v28
	v_and_b32_e32 v27, 0xffff0000, v28
	v_lshlrev_b32_e32 v28, 16, v29
	v_and_b32_e32 v29, 0xffff0000, v29
	v_pk_fma_f32 v[24:25], v[90:91], v[8:9], v[24:25]
	v_pk_fma_f32 v[22:23], v[88:89], v[6:7], v[22:23]
	v_pk_fma_f32 v[28:29], v[82:83], v[4:5], v[28:29]
	v_pk_fma_f32 v[26:27], v[80:81], v[2:3], v[26:27]
	v_cvt_pk_bf16_f32 v22, v22, v23
	v_cvt_pk_bf16_f32 v23, v24, v25
	v_cvt_pk_bf16_f32 v24, v26, v27
	v_cvt_pk_bf16_f32 v25, v28, v29
	global_store_dwordx4 v[120:121], v[22:25], off offset:256
	s_waitcnt vmcnt(7)
	v_lshlrev_b32_e32 v26, 16, v32
	v_and_b32_e32 v27, 0xffff0000, v32
	v_lshlrev_b32_e32 v22, 16, v30
	v_and_b32_e32 v23, 0xffff0000, v30
	v_lshlrev_b32_e32 v24, 16, v31
	v_and_b32_e32 v25, 0xffff0000, v31
	v_lshlrev_b32_e32 v28, 16, v33
	v_and_b32_e32 v29, 0xffff0000, v33
	v_pk_fma_f32 v[24:25], v[86:87], v[16:17], v[24:25]
	v_pk_fma_f32 v[22:23], v[84:85], v[14:15], v[22:23]
	v_pk_fma_f32 v[28:29], v[78:79], v[12:13], v[28:29]
	v_pk_fma_f32 v[26:27], v[76:77], v[10:11], v[26:27]
	v_cvt_pk_bf16_f32 v22, v22, v23
	v_cvt_pk_bf16_f32 v23, v24, v25
	v_cvt_pk_bf16_f32 v24, v26, v27
	v_cvt_pk_bf16_f32 v25, v28, v29
	global_store_dwordx4 v[126:127], v[22:25], off
	s_waitcnt vmcnt(7)
	v_lshlrev_b32_e32 v26, 16, v102
	v_and_b32_e32 v27, 0xffff0000, v102
	v_lshlrev_b32_e32 v22, 16, v100
	v_and_b32_e32 v23, 0xffff0000, v100
	v_lshlrev_b32_e32 v24, 16, v101
	v_and_b32_e32 v25, 0xffff0000, v101
	v_lshlrev_b32_e32 v28, 16, v103
	v_and_b32_e32 v29, 0xffff0000, v103
	v_pk_fma_f32 v[24:25], v[74:75], v[8:9], v[24:25]
	v_pk_fma_f32 v[22:23], v[72:73], v[6:7], v[22:23]
	v_pk_fma_f32 v[28:29], v[66:67], v[4:5], v[28:29]
	v_pk_fma_f32 v[26:27], v[64:65], v[2:3], v[26:27]
	v_cvt_pk_bf16_f32 v22, v22, v23
	v_cvt_pk_bf16_f32 v23, v24, v25
	v_cvt_pk_bf16_f32 v24, v26, v27
	v_cvt_pk_bf16_f32 v25, v28, v29
	global_store_dwordx4 v[124:125], v[22:25], off offset:256
	s_waitcnt vmcnt(7)
	v_lshlrev_b32_e32 v26, 16, v106
	v_and_b32_e32 v27, 0xffff0000, v106
	v_lshlrev_b32_e32 v22, 16, v104
	v_and_b32_e32 v23, 0xffff0000, v104
	v_lshlrev_b32_e32 v24, 16, v105
	v_and_b32_e32 v25, 0xffff0000, v105
	v_lshlrev_b32_e32 v28, 16, v107
	v_and_b32_e32 v29, 0xffff0000, v107
	v_pk_fma_f32 v[24:25], v[70:71], v[16:17], v[24:25]
	v_pk_fma_f32 v[22:23], v[68:69], v[14:15], v[22:23]
	v_pk_fma_f32 v[28:29], v[62:63], v[12:13], v[28:29]
	v_pk_fma_f32 v[26:27], v[60:61], v[10:11], v[26:27]
	v_cvt_pk_bf16_f32 v22, v22, v23
	v_cvt_pk_bf16_f32 v23, v24, v25
	v_cvt_pk_bf16_f32 v24, v26, v27
	v_cvt_pk_bf16_f32 v25, v28, v29
	global_store_dwordx4 v[130:131], v[22:25], off
	s_waitcnt vmcnt(7)
	v_lshlrev_b32_e32 v26, 16, v110
	v_and_b32_e32 v27, 0xffff0000, v110
	v_lshlrev_b32_e32 v22, 16, v108
	v_and_b32_e32 v23, 0xffff0000, v108
	v_lshlrev_b32_e32 v24, 16, v109
	v_and_b32_e32 v25, 0xffff0000, v109
	v_lshlrev_b32_e32 v28, 16, v111
	v_and_b32_e32 v29, 0xffff0000, v111
	v_pk_fma_f32 v[24:25], v[58:59], v[8:9], v[24:25]
	v_pk_fma_f32 v[22:23], v[56:57], v[6:7], v[22:23]
	v_pk_fma_f32 v[28:29], v[50:51], v[4:5], v[28:29]
	v_pk_fma_f32 v[26:27], v[48:49], v[2:3], v[26:27]
	v_cvt_pk_bf16_f32 v22, v22, v23
	v_cvt_pk_bf16_f32 v23, v24, v25
	v_cvt_pk_bf16_f32 v24, v26, v27
	v_cvt_pk_bf16_f32 v25, v28, v29
	global_store_dwordx4 v[128:129], v[22:25], off offset:256
	s_waitcnt vmcnt(7)
	v_lshlrev_b32_e32 v26, 16, v114
	v_and_b32_e32 v27, 0xffff0000, v114
	v_lshlrev_b32_e32 v22, 16, v112
	v_and_b32_e32 v23, 0xffff0000, v112
	v_lshlrev_b32_e32 v24, 16, v113
	v_and_b32_e32 v25, 0xffff0000, v113
	v_lshlrev_b32_e32 v28, 16, v115
	v_and_b32_e32 v29, 0xffff0000, v115
	v_pk_fma_f32 v[16:17], v[54:55], v[16:17], v[24:25]
	v_pk_fma_f32 v[14:15], v[52:53], v[14:15], v[22:23]
	v_pk_fma_f32 v[22:23], v[46:47], v[12:13], v[28:29]
	v_pk_fma_f32 v[12:13], v[44:45], v[10:11], v[26:27]
	v_cvt_pk_bf16_f32 v10, v14, v15
	v_cvt_pk_bf16_f32 v11, v16, v17
	v_cvt_pk_bf16_f32 v12, v12, v13
	v_cvt_pk_bf16_f32 v13, v22, v23
	global_store_dwordx4 v[18:19], v[10:13], off
	s_waitcnt vmcnt(7)
	v_lshlrev_b32_e32 v14, 16, v118
	v_and_b32_e32 v15, 0xffff0000, v118
	v_lshlrev_b32_e32 v10, 16, v116
	v_and_b32_e32 v11, 0xffff0000, v116
	v_lshlrev_b32_e32 v12, 16, v117
	v_and_b32_e32 v13, 0xffff0000, v117
	v_lshlrev_b32_e32 v16, 16, v119
	v_and_b32_e32 v17, 0xffff0000, v119
	v_pk_fma_f32 v[8:9], v[42:43], v[8:9], v[12:13]
	v_pk_fma_f32 v[6:7], v[40:41], v[6:7], v[10:11]
	v_pk_fma_f32 v[10:11], v[38:39], v[4:5], v[16:17]
	v_pk_fma_f32 v[4:5], v[36:37], v[2:3], v[14:15]
	v_cvt_pk_bf16_f32 v2, v6, v7
	v_cvt_pk_bf16_f32 v3, v8, v9
	v_cvt_pk_bf16_f32 v4, v4, v5
	v_cvt_pk_bf16_f32 v5, v10, v11
	global_store_dwordx4 v[20:21], v[2:5], off offset:256
	s_and_b64 vcc, exec, s[38:39]
	s_mov_b32 s77, s73
	s_mov_b32 s78, s76
	s_mov_b64 s[40:41], s[18:19]
	s_mov_b64 s[36:37], s[2:3]
	s_cbranch_vccz .LBB0_993
	s_waitcnt vmcnt(0)
	v_readlane_b32 s64, v255, 32
	v_readlane_b32 s72, v255, 34
	s_cmpk_gt_u32 s14, 0xff
	v_readlane_b32 s65, v255, 33
	v_readlane_b32 s73, v255, 35
	v_readlane_b32 s71, v255, 36
	s_cbranch_scc1 .LBB0_1000
	s_barrier

.LBB0_1016:
	s_lshr_b32 s20, s20, 11
	s_and_b64 s[14:15], s[14:15], exec
	s_cselect_b32 s14, 32, s20
	s_lshl_b64 s[0:1], s[0:1], 11
	s_mul_hi_u32 s15, s14, 0x6000
	s_mulk_i32 s14, 0x6000
	v_lshl_or_b32 v164, s83, 8, v171
	s_add_u32 s14, s76, s14
	s_addc_u32 s15, s77, s15
	v_ashrrev_i32_e32 v165, 31, v164
	v_lshl_add_u64 v[136:137], v[164:165], 2, s[14:15]
	global_load_dwordx4 v[140:143], v[136:137], off offset:16
	global_load_dwordx4 v[144:147], v[136:137], off
	global_load_dwordx4 v[132:135], v[136:137], off offset:528
	s_nop 0
	global_load_dwordx4 v[136:139], v[136:137], off offset:512
	s_add_u32 s14, s72, s0
	v_readlane_b32 s46, v255, 41
	s_addc_u32 s15, s73, s1
	v_add_u32_e32 v162, s48, v35
	v_readlane_b32 s47, v255, 42
	s_mov_b64 s[0:1], -1
	s_and_b64 vcc, exec, s[46:47]
	v_ashrrev_i32_e32 v163, 31, v162
	v_lshl_add_u64 v[160:161], v[164:165], 1, s[14:15]
	s_cbranch_vccz .LBB0_1018
	v_lshlrev_b64 v[166:167], 11, v[162:163]
	v_lshl_add_u64 v[166:167], v[160:161], 0, v[166:167]
	s_mov_b64 s[0:1], 0x8000
	v_lshl_add_u64 v[206:207], v[166:167], 0, s[0:1]
	v_add_co_u32_e32 v208, vcc, 0x8000, v166
	s_mov_b64 s[0:1], 0x10000
	s_nop 0
	v_addc_co_u32_e32 v209, vcc, 0, v167, vcc
	v_lshl_add_u64 v[210:211], v[166:167], 0, s[0:1]
	s_mov_b32 s0, 0x10000
	v_add_co_u32_e32 v214, vcc, s0, v166
	s_mov_b64 s[0:1], 0x18000
	s_nop 0
	v_addc_co_u32_e32 v215, vcc, 0, v167, vcc
	v_lshl_add_u64 v[168:169], v[166:167], 0, s[0:1]
	s_mov_b32 s0, 0x18000
	v_add_co_u32_e32 v218, vcc, s0, v166
	global_load_dwordx4 v[174:177], v[166:167], off
	global_load_dwordx4 v[178:181], v[166:167], off offset:256
	v_addc_co_u32_e32 v219, vcc, 0, v167, vcc
	global_load_dwordx4 v[182:185], v[208:209], off
	global_load_dwordx4 v[186:189], v[206:207], off offset:256
	global_load_dwordx4 v[190:193], v[214:215], off
	global_load_dwordx4 v[194:197], v[210:211], off offset:256
	global_load_dwordx4 v[198:201], v[218:219], off
	global_load_dwordx4 v[202:205], v[168:169], off offset:256
	s_waitcnt vmcnt(7)
	v_lshlrev_b32_e32 v220, 16, v174
	v_and_b32_e32 v221, 0xffff0000, v174
	v_lshlrev_b32_e32 v174, 16, v175
	v_and_b32_e32 v175, 0xffff0000, v175
	v_lshlrev_b32_e32 v222, 16, v176
	v_and_b32_e32 v223, 0xffff0000, v176
	v_lshlrev_b32_e32 v176, 16, v177
	v_and_b32_e32 v177, 0xffff0000, v177
	v_pk_fma_f32 v[224:225], v[130:131], v[146:147], v[174:175]
	v_pk_fma_f32 v[174:175], v[128:129], v[144:145], v[220:221]
	v_pk_fma_f32 v[220:221], v[126:127], v[142:143], v[176:177]
	v_pk_fma_f32 v[176:177], v[124:125], v[140:141], v[222:223]
	v_cvt_pk_bf16_f32 v174, v174, v175
	v_cvt_pk_bf16_f32 v175, v224, v225
	v_cvt_pk_bf16_f32 v176, v176, v177
	v_cvt_pk_bf16_f32 v177, v220, v221
	global_store_dwordx4 v[166:167], v[174:177], off
	s_nop 1
	s_waitcnt vmcnt(7)
	v_lshlrev_b32_e32 v174, 16, v178
	v_and_b32_e32 v175, 0xffff0000, v178
	v_lshlrev_b32_e32 v176, 16, v179
	v_and_b32_e32 v177, 0xffff0000, v179
	v_lshlrev_b32_e32 v178, 16, v180
	v_and_b32_e32 v179, 0xffff0000, v180
	v_lshlrev_b32_e32 v180, 16, v181
	v_and_b32_e32 v181, 0xffff0000, v181
	v_pk_fma_f32 v[176:177], v[122:123], v[138:139], v[176:177]
	v_pk_fma_f32 v[174:175], v[120:121], v[136:137], v[174:175]
	v_pk_fma_f32 v[180:181], v[114:115], v[134:135], v[180:181]
	v_pk_fma_f32 v[178:179], v[112:113], v[132:133], v[178:179]
	v_cvt_pk_bf16_f32 v174, v174, v175
	v_cvt_pk_bf16_f32 v175, v176, v177
	v_cvt_pk_bf16_f32 v176, v178, v179
	v_cvt_pk_bf16_f32 v177, v180, v181
	global_store_dwordx4 v[166:167], v[174:177], off offset:256
	s_waitcnt vmcnt(7)
	v_lshlrev_b32_e32 v178, 16, v184
	v_and_b32_e32 v179, 0xffff0000, v184
	v_lshlrev_b32_e32 v174, 16, v182
	v_and_b32_e32 v175, 0xffff0000, v182
	v_lshlrev_b32_e32 v176, 16, v183
	v_and_b32_e32 v177, 0xffff0000, v183
	v_lshlrev_b32_e32 v180, 16, v185
	v_and_b32_e32 v181, 0xffff0000, v185
	v_pk_fma_f32 v[176:177], v[118:119], v[146:147], v[176:177]
	v_pk_fma_f32 v[174:175], v[116:117], v[144:145], v[174:175]
	v_pk_fma_f32 v[180:181], v[110:111], v[142:143], v[180:181]
	v_pk_fma_f32 v[178:179], v[108:109], v[140:141], v[178:179]
	v_cvt_pk_bf16_f32 v174, v174, v175
	v_cvt_pk_bf16_f32 v175, v176, v177
	v_cvt_pk_bf16_f32 v176, v178, v179
	v_cvt_pk_bf16_f32 v177, v180, v181
	global_store_dwordx4 v[208:209], v[174:177], off
	s_waitcnt vmcnt(7)
	v_lshlrev_b32_e32 v178, 16, v188
	v_and_b32_e32 v179, 0xffff0000, v188
	v_lshlrev_b32_e32 v174, 16, v186
	v_and_b32_e32 v175, 0xffff0000, v186
	v_lshlrev_b32_e32 v176, 16, v187
	v_and_b32_e32 v177, 0xffff0000, v187
	v_lshlrev_b32_e32 v180, 16, v189
	v_and_b32_e32 v181, 0xffff0000, v189
	v_pk_fma_f32 v[176:177], v[106:107], v[138:139], v[176:177]
	v_pk_fma_f32 v[174:175], v[104:105], v[136:137], v[174:175]
	v_pk_fma_f32 v[180:181], v[102:103], v[134:135], v[180:181]
	v_pk_fma_f32 v[178:179], v[100:101], v[132:133], v[178:179]
	v_cvt_pk_bf16_f32 v174, v174, v175
	v_cvt_pk_bf16_f32 v175, v176, v177
	v_cvt_pk_bf16_f32 v176, v178, v179
	v_cvt_pk_bf16_f32 v177, v180, v181
	global_store_dwordx4 v[206:207], v[174:177], off offset:256
	s_waitcnt vmcnt(7)
	v_lshlrev_b32_e32 v178, 16, v192
	v_and_b32_e32 v179, 0xffff0000, v192
	v_lshlrev_b32_e32 v174, 16, v190
	v_and_b32_e32 v175, 0xffff0000, v190
	v_lshlrev_b32_e32 v176, 16, v191
	v_and_b32_e32 v177, 0xffff0000, v191
	v_lshlrev_b32_e32 v180, 16, v193
	v_and_b32_e32 v181, 0xffff0000, v193
	v_pk_fma_f32 v[176:177], v[98:99], v[146:147], v[176:177]
	v_pk_fma_f32 v[174:175], v[96:97], v[144:145], v[174:175]
	v_pk_fma_f32 v[180:181], v[94:95], v[142:143], v[180:181]
	v_pk_fma_f32 v[178:179], v[92:93], v[140:141], v[178:179]
	v_cvt_pk_bf16_f32 v174, v174, v175
	v_cvt_pk_bf16_f32 v175, v176, v177
	v_cvt_pk_bf16_f32 v176, v178, v179
	v_cvt_pk_bf16_f32 v177, v180, v181
	global_store_dwordx4 v[214:215], v[174:177], off
	s_waitcnt vmcnt(7)
	v_lshlrev_b32_e32 v178, 16, v196
	v_and_b32_e32 v179, 0xffff0000, v196
	v_lshlrev_b32_e32 v174, 16, v194
	v_and_b32_e32 v175, 0xffff0000, v194
	v_lshlrev_b32_e32 v176, 16, v195
	v_and_b32_e32 v177, 0xffff0000, v195
	v_lshlrev_b32_e32 v180, 16, v197
	v_and_b32_e32 v181, 0xffff0000, v197
	v_pk_fma_f32 v[176:177], v[90:91], v[138:139], v[176:177]
	v_pk_fma_f32 v[174:175], v[88:89], v[136:137], v[174:175]
	v_pk_fma_f32 v[180:181], v[82:83], v[134:135], v[180:181]
	v_pk_fma_f32 v[178:179], v[80:81], v[132:133], v[178:179]
	v_cvt_pk_bf16_f32 v174, v174, v175
	v_cvt_pk_bf16_f32 v175, v176, v177
	v_cvt_pk_bf16_f32 v176, v178, v179
	v_cvt_pk_bf16_f32 v177, v180, v181
	global_store_dwordx4 v[210:211], v[174:177], off offset:256
	s_waitcnt vmcnt(7)
	v_lshlrev_b32_e32 v178, 16, v200
	v_and_b32_e32 v179, 0xffff0000, v200
	v_lshlrev_b32_e32 v174, 16, v198
	v_and_b32_e32 v175, 0xffff0000, v198
	v_lshlrev_b32_e32 v176, 16, v199
	v_and_b32_e32 v177, 0xffff0000, v199
	v_lshlrev_b32_e32 v180, 16, v201
	v_and_b32_e32 v181, 0xffff0000, v201
	v_pk_fma_f32 v[176:177], v[86:87], v[146:147], v[176:177]
	v_pk_fma_f32 v[174:175], v[84:85], v[144:145], v[174:175]
	v_pk_fma_f32 v[180:181], v[78:79], v[142:143], v[180:181]
	v_pk_fma_f32 v[178:179], v[76:77], v[140:141], v[178:179]
	v_cvt_pk_bf16_f32 v174, v174, v175
	v_cvt_pk_bf16_f32 v175, v176, v177
	v_cvt_pk_bf16_f32 v176, v178, v179
	v_cvt_pk_bf16_f32 v177, v180, v181
	global_store_dwordx4 v[218:219], v[174:177], off
	s_waitcnt vmcnt(7)
	v_lshlrev_b32_e32 v178, 16, v204
	v_and_b32_e32 v179, 0xffff0000, v204
	v_lshlrev_b32_e32 v174, 16, v202
	v_and_b32_e32 v175, 0xffff0000, v202
	v_lshlrev_b32_e32 v176, 16, v203
	v_and_b32_e32 v177, 0xffff0000, v203
	v_lshlrev_b32_e32 v180, 16, v205
	v_and_b32_e32 v181, 0xffff0000, v205
	v_pk_fma_f32 v[176:177], v[74:75], v[138:139], v[176:177]
	v_pk_fma_f32 v[174:175], v[72:73], v[136:137], v[174:175]
	v_pk_fma_f32 v[180:181], v[70:71], v[134:135], v[180:181]
	v_pk_fma_f32 v[178:179], v[68:69], v[132:133], v[178:179]
	v_cvt_pk_bf16_f32 v174, v174, v175
	v_cvt_pk_bf16_f32 v175, v176, v177
	v_cvt_pk_bf16_f32 v176, v178, v179
	v_cvt_pk_bf16_f32 v177, v180, v181
	global_store_dwordx4 v[168:169], v[174:177], off offset:256
	s_mov_b64 s[0:1], 0x40000
	v_lshl_add_u64 v[206:207], v[166:167], 0, s[0:1]
	s_mov_b32 s0, 0x40000
	v_add_co_u32_e32 v208, vcc, s0, v166
	s_mov_b64 s[0:1], 0x48000
	s_nop 0
	v_addc_co_u32_e32 v209, vcc, 0, v167, vcc
	v_lshl_add_u64 v[210:211], v[166:167], 0, s[0:1]
	s_mov_b32 s0, 0x48000
	v_add_co_u32_e32 v214, vcc, s0, v166
	s_mov_b64 s[0:1], 0x50000
	s_nop 0
	v_addc_co_u32_e32 v215, vcc, 0, v167, vcc
	v_lshl_add_u64 v[218:219], v[166:167], 0, s[0:1]
	s_mov_b32 s0, 0x50000
	v_add_co_u32_e32 v220, vcc, s0, v166
	s_mov_b64 s[0:1], 0x58000
	s_nop 0
	v_addc_co_u32_e32 v221, vcc, 0, v167, vcc
	v_lshl_add_u64 v[168:169], v[166:167], 0, s[0:1]
	s_mov_b32 s0, 0x58000
	v_add_co_u32_e32 v166, vcc, s0, v166
	global_load_dwordx4 v[174:177], v[208:209], off
	global_load_dwordx4 v[178:181], v[206:207], off offset:256
	v_addc_co_u32_e32 v167, vcc, 0, v167, vcc
	global_load_dwordx4 v[182:185], v[214:215], off
	global_load_dwordx4 v[186:189], v[210:211], off offset:256
	global_load_dwordx4 v[190:193], v[220:221], off
	global_load_dwordx4 v[194:197], v[218:219], off offset:256
	global_load_dwordx4 v[198:201], v[166:167], off
	global_load_dwordx4 v[202:205], v[168:169], off offset:256
	s_waitcnt vmcnt(7)
	v_lshlrev_b32_e32 v222, 16, v174
	v_and_b32_e32 v223, 0xffff0000, v174
	v_lshlrev_b32_e32 v174, 16, v175
	v_and_b32_e32 v175, 0xffff0000, v175
	v_lshlrev_b32_e32 v224, 16, v176
	v_and_b32_e32 v225, 0xffff0000, v176
	v_lshlrev_b32_e32 v176, 16, v177
	v_and_b32_e32 v177, 0xffff0000, v177
	v_pk_fma_f32 v[226:227], v[66:67], v[146:147], v[174:175]
	v_pk_fma_f32 v[174:175], v[64:65], v[144:145], v[222:223]
	v_pk_fma_f32 v[222:223], v[62:63], v[142:143], v[176:177]
	v_pk_fma_f32 v[176:177], v[60:61], v[140:141], v[224:225]
	v_cvt_pk_bf16_f32 v174, v174, v175
	v_cvt_pk_bf16_f32 v175, v226, v227
	v_cvt_pk_bf16_f32 v176, v176, v177
	v_cvt_pk_bf16_f32 v177, v222, v223
	global_store_dwordx4 v[208:209], v[174:177], off
	s_nop 1
	s_waitcnt vmcnt(7)
	v_lshlrev_b32_e32 v174, 16, v178
	v_and_b32_e32 v175, 0xffff0000, v178
	v_lshlrev_b32_e32 v176, 16, v179
	v_and_b32_e32 v177, 0xffff0000, v179
	v_lshlrev_b32_e32 v178, 16, v180
	v_and_b32_e32 v179, 0xffff0000, v180
	v_lshlrev_b32_e32 v180, 16, v181
	v_and_b32_e32 v181, 0xffff0000, v181
	v_pk_fma_f32 v[176:177], v[54:55], v[138:139], v[176:177]
	v_pk_fma_f32 v[174:175], v[52:53], v[136:137], v[174:175]
	v_pk_fma_f32 v[180:181], v[46:47], v[134:135], v[180:181]
	v_pk_fma_f32 v[178:179], v[44:45], v[132:133], v[178:179]
	v_cvt_pk_bf16_f32 v174, v174, v175
	v_cvt_pk_bf16_f32 v175, v176, v177
	v_cvt_pk_bf16_f32 v176, v178, v179
	v_cvt_pk_bf16_f32 v177, v180, v181
	global_store_dwordx4 v[206:207], v[174:177], off offset:256
	s_waitcnt vmcnt(7)
	v_lshlrev_b32_e32 v178, 16, v184
	v_and_b32_e32 v179, 0xffff0000, v184
	v_lshlrev_b32_e32 v174, 16, v182
	v_and_b32_e32 v175, 0xffff0000, v182
	v_lshlrev_b32_e32 v176, 16, v183
	v_and_b32_e32 v177, 0xffff0000, v183
	v_lshlrev_b32_e32 v180, 16, v185
	v_and_b32_e32 v181, 0xffff0000, v185
	v_pk_fma_f32 v[176:177], v[58:59], v[146:147], v[176:177]
	v_pk_fma_f32 v[174:175], v[56:57], v[144:145], v[174:175]
	v_pk_fma_f32 v[180:181], v[50:51], v[142:143], v[180:181]
	v_pk_fma_f32 v[178:179], v[48:49], v[140:141], v[178:179]
	v_cvt_pk_bf16_f32 v174, v174, v175
	v_cvt_pk_bf16_f32 v175, v176, v177
	v_cvt_pk_bf16_f32 v176, v178, v179
	v_cvt_pk_bf16_f32 v177, v180, v181
	global_store_dwordx4 v[214:215], v[174:177], off
	s_waitcnt vmcnt(7)
	v_lshlrev_b32_e32 v178, 16, v188
	v_and_b32_e32 v179, 0xffff0000, v188
	v_lshlrev_b32_e32 v174, 16, v186
	v_and_b32_e32 v175, 0xffff0000, v186
	v_lshlrev_b32_e32 v176, 16, v187
	v_and_b32_e32 v177, 0xffff0000, v187
	v_lshlrev_b32_e32 v180, 16, v189
	v_and_b32_e32 v181, 0xffff0000, v189
	v_pk_fma_f32 v[176:177], v[42:43], v[138:139], v[176:177]
	v_pk_fma_f32 v[174:175], v[40:41], v[136:137], v[174:175]
	v_pk_fma_f32 v[180:181], v[38:39], v[134:135], v[180:181]
	v_pk_fma_f32 v[178:179], v[36:37], v[132:133], v[178:179]
	v_cvt_pk_bf16_f32 v174, v174, v175
	v_cvt_pk_bf16_f32 v175, v176, v177
	v_cvt_pk_bf16_f32 v176, v178, v179
	v_cvt_pk_bf16_f32 v177, v180, v181
	global_store_dwordx4 v[210:211], v[174:177], off offset:256
	s_waitcnt vmcnt(7)
	v_lshlrev_b32_e32 v178, 16, v192
	v_and_b32_e32 v179, 0xffff0000, v192
	v_lshlrev_b32_e32 v174, 16, v190
	v_and_b32_e32 v175, 0xffff0000, v190
	v_lshlrev_b32_e32 v176, 16, v191
	v_and_b32_e32 v177, 0xffff0000, v191
	v_lshlrev_b32_e32 v180, 16, v193
	v_and_b32_e32 v181, 0xffff0000, v193
	v_pk_fma_f32 v[176:177], v[32:33], v[146:147], v[176:177]
	v_pk_fma_f32 v[174:175], v[30:31], v[144:145], v[174:175]
	v_pk_fma_f32 v[180:181], v[28:29], v[142:143], v[180:181]
	v_pk_fma_f32 v[178:179], v[26:27], v[140:141], v[178:179]
	v_cvt_pk_bf16_f32 v174, v174, v175
	v_cvt_pk_bf16_f32 v175, v176, v177
	v_cvt_pk_bf16_f32 v176, v178, v179
	v_cvt_pk_bf16_f32 v177, v180, v181
	global_store_dwordx4 v[220:221], v[174:177], off
	s_waitcnt vmcnt(7)
	v_lshlrev_b32_e32 v178, 16, v196
	v_and_b32_e32 v179, 0xffff0000, v196
	v_lshlrev_b32_e32 v174, 16, v194
	v_and_b32_e32 v175, 0xffff0000, v194
	v_lshlrev_b32_e32 v176, 16, v195
	v_and_b32_e32 v177, 0xffff0000, v195
	v_lshlrev_b32_e32 v180, 16, v197
	v_and_b32_e32 v181, 0xffff0000, v197
	v_pk_fma_f32 v[176:177], v[20:21], v[138:139], v[176:177]
	v_pk_fma_f32 v[174:175], v[18:19], v[136:137], v[174:175]
	v_pk_fma_f32 v[180:181], v[12:13], v[134:135], v[180:181]
	v_pk_fma_f32 v[178:179], v[10:11], v[132:133], v[178:179]
	v_cvt_pk_bf16_f32 v174, v174, v175
	v_cvt_pk_bf16_f32 v175, v176, v177
	v_cvt_pk_bf16_f32 v176, v178, v179
	v_cvt_pk_bf16_f32 v177, v180, v181
	global_store_dwordx4 v[218:219], v[174:177], off offset:256
	s_waitcnt vmcnt(7)
	v_lshlrev_b32_e32 v178, 16, v200
	v_and_b32_e32 v179, 0xffff0000, v200
	v_lshlrev_b32_e32 v174, 16, v198
	v_and_b32_e32 v175, 0xffff0000, v198
	v_lshlrev_b32_e32 v176, 16, v199
	v_and_b32_e32 v177, 0xffff0000, v199
	v_lshlrev_b32_e32 v180, 16, v201
	v_and_b32_e32 v181, 0xffff0000, v201
	v_pk_fma_f32 v[176:177], v[24:25], v[146:147], v[176:177]
	v_pk_fma_f32 v[174:175], v[22:23], v[144:145], v[174:175]
	v_pk_fma_f32 v[180:181], v[16:17], v[142:143], v[180:181]
	v_pk_fma_f32 v[178:179], v[14:15], v[140:141], v[178:179]
	v_cvt_pk_bf16_f32 v174, v174, v175
	v_cvt_pk_bf16_f32 v175, v176, v177
	v_cvt_pk_bf16_f32 v176, v178, v179
	v_cvt_pk_bf16_f32 v177, v180, v181
	global_store_dwordx4 v[166:167], v[174:177], off
	s_waitcnt vmcnt(7)
	v_lshlrev_b32_e32 v166, 16, v202
	v_and_b32_e32 v167, 0xffff0000, v202
	v_lshlrev_b32_e32 v174, 16, v203
	v_and_b32_e32 v175, 0xffff0000, v203
	v_lshlrev_b32_e32 v176, 16, v204
	v_and_b32_e32 v177, 0xffff0000, v204
	v_lshlrev_b32_e32 v178, 16, v205
	v_and_b32_e32 v179, 0xffff0000, v205
	v_pk_fma_f32 v[180:181], v[8:9], v[138:139], v[174:175]
	v_pk_fma_f32 v[166:167], v[6:7], v[136:137], v[166:167]
	v_pk_fma_f32 v[178:179], v[4:5], v[134:135], v[178:179]
	v_pk_fma_f32 v[176:177], v[2:3], v[132:133], v[176:177]
	v_cvt_pk_bf16_f32 v174, v166, v167
	v_cvt_pk_bf16_f32 v175, v180, v181
	v_cvt_pk_bf16_f32 v176, v176, v177
	v_cvt_pk_bf16_f32 v177, v178, v179
	global_store_dwordx4 v[168:169], v[174:177], off offset:256
	s_mov_b64 s[0:1], 0
